# P9 gate-up epilogue rewritten: bias folded into accumulator init, packed f32 math, permlane16_swap paired 16B stores
# speedup vs baseline: 1.0137x; 1.0137x over previous
.LBB0_1325:
	s_lshl_b32 s4, s4, 5
	s_and_b32 s18, s4, 0x60
	s_lshl_b32 s13, s12, 13
	s_lshl_b32 s19, s18, 7
	s_add_u32 s4, s8, 0x34e00000
	s_addc_u32 s5, s9, 0
	s_add_u32 s8, s8, 0x70700080
	s_addc_u32 s9, s9, 0
	s_lshl_b32 s10, s18, 2
	s_add_i32 s20, s10, 0
	s_mov_b64 s[10:11], 0x80
	s_add_i32 s36, s27, 0x18000
	v_lshl_add_u64 v[2:3], v[2:3], 0, s[10:11]
	s_mov_b32 m0, s36
	s_add_i32 s37, s27, 0x1a000
	s_waitcnt vmcnt(4)
	s_barrier
	global_load_lds_dwordx4 v[2:3], off
	v_lshl_add_u64 v[0:1], v[0:1], 0, s[10:11]
	s_mov_b32 m0, s37
	s_add_i32 s38, s27, 0x8000
	s_add_i32 s39, s27, 0xa000
	global_load_lds_dwordx4 v[0:1], off
	v_lshl_add_u64 v[0:1], s[8:9], 0, v[156:157]
	s_mov_b32 m0, s38
	s_add_u32 s14, s16, 0x40080
	global_load_lds_dwordx4 v[0:1], off
	v_lshl_add_u64 v[0:1], s[8:9], 0, v[166:167]
	s_mov_b32 m0, s39
	s_addc_u32 s15, s17, 0
	s_add_i32 s40, s27, 0x1c000
	global_load_lds_dwordx4 v[0:1], off
	v_lshl_add_u64 v[0:1], s[14:15], 0, v[154:155]
	s_mov_b32 m0, s40
	s_add_i32 s41, s27, 0x1e000
	global_load_lds_dwordx4 v[0:1], off
	v_lshl_add_u64 v[0:1], s[14:15], 0, v[152:153]
	s_mov_b32 m0, s41
	v_lshlrev_b32_e32 v3, 2, v8
	global_load_lds_dwordx4 v[0:1], off
	v_lshrrev_b32_e32 v1, 1, v8
	v_and_b32_e32 v0, 15, v8
	v_and_b32_e32 v1, 24, v1
	v_lshlrev_b32_e32 v2, 1, v1
	v_lshl_or_b32 v167, s12, 6, v0
	v_lshlrev_b32_e32 v0, 6, v0
	v_and_b32_e32 v3, 32, v3
	v_bitop3_b32 v0, v0, v3, v2 bitop3:0x36
	s_waitcnt vmcnt(6)
	s_add_i32 s19, s19, 0
	v_add_u32_e32 v2, s19, v0
	v_add_u32_e32 v0, 0, v0
	s_add_i32 s20, s20, 0x22a00
	s_mov_b32 s52, 0
	v_add_u32_e32 v184, 0x10000, v2
	v_add_u32_e32 v185, 0x14000, v2
	v_add_u32_e32 v186, 0x18000, v2
	v_add_u32_e32 v187, 0x1c000, v2
	v_lshl_add_u32 v188, v1, 2, s20
	v_add_u32_e32 v189, 0x10400, v2
	v_add_u32_e32 v190, 0x10800, v2
	v_add_u32_e32 v191, 0x10c00, v2
	v_add_u32_e32 v192, 0x14400, v2
	v_add_u32_e32 v193, 0x14800, v2
	v_add_u32_e32 v194, 0x14c00, v2
	v_add_u32_e32 v195, 0x18400, v2
	v_add_u32_e32 v196, 0x18800, v2
	v_add_u32_e32 v197, 0x18c00, v2
	v_add_u32_e32 v198, 0x1c400, v2
	v_add_u32_e32 v199, 0x1c800, v2
	v_add_u32_e32 v200, 0x1cc00, v2
	v_or_b32_e32 v201, s18, v1
	v_add_u32_e32 v202, s13, v0
	v_mov_b32_e32 v203, 0x7a7a7a7a
	v_mov_b32_e32 v209, 0x7c7c7c7c
	s_mov_b32 s62, 0xc01d265f
	s_mov_b32 s63, 0xc01d265f
	s_mov_b32 s65, 0x40e00000
	s_mov_b64 s[58:59], 0x10000
	s_mov_b32 s60, 0x30000
	s_mov_b32 s61, 0
	v_mov_b32_e32 v204, 0x7f7f7f7f
	s_mov_b32 s42, 0xc1c00000
	s_mov_b32 s43, 0x40000
	s_mov_b32 s44, 0x48000
	s_mov_b32 s45, 0x50000
	v_mov_b32_e32 v205, 0x42000000
	v_mov_b32_e32 v208, v156
	s_mov_b32 s46, 0
	s_barrier
	s_branch .LBB0_1327
.LBB0_1326:
	s_nop 15
	s_nop 15
	v_lshl_add_u32 v20, s50, 8, v167
	v_lshl_or_b32 v18, s51, 7, v201
	v_ashrrev_i32_e32 v21, 31, v20
	v_ashrrev_i32_e32 v19, 31, v18
	v_lshlrev_b64 v[16:17], 11, v[20:21]
	v_lshl_add_u64 v[16:17], s[4:5], 0, v[16:17]
	v_lshl_add_u64 v[16:17], v[16:17], 0, v[18:19]
	v_mbcnt_lo_u32_b32 v20, -1, 0
	v_mbcnt_hi_u32_b32 v20, -1, v20
	v_and_b32_e32 v20, 16, v20
	v_mov_b32_e32 v18, 0x8000
	v_cmp_eq_u32_e32 vcc, 0, v20
	s_nop 1
	v_cndmask_b32_e32 v18, -8, v18, vcc
	v_ashrrev_i32_e32 v19, 31, v18
	v_lshl_add_u64 v[16:17], v[16:17], 0, v[18:19]
	v_min_f32_e32 v132, s65, v132
	v_min_f32_e32 v133, s65, v133
	v_min_f32_e32 v134, s65, v134
	v_min_f32_e32 v135, s65, v135
	v_min_f32_e32 v124, s65, v124
	v_min_f32_e32 v125, s65, v125
	v_min_f32_e32 v126, s65, v126
	v_min_f32_e32 v127, s65, v127
	v_pk_mul_f32 v[0:1], v[132:133], s[62:63]
	v_pk_mul_f32 v[2:3], v[134:135], s[62:63]
	v_pk_mul_f32 v[4:5], v[124:125], s[62:63]
	v_pk_mul_f32 v[6:7], v[126:127], s[62:63]
	v_exp_f32_e32 v0, v0
	v_exp_f32_e32 v1, v1
	v_exp_f32_e32 v2, v2
	v_exp_f32_e32 v3, v3
	v_exp_f32_e32 v4, v4
	v_exp_f32_e32 v5, v5
	v_exp_f32_e32 v6, v6
	v_exp_f32_e32 v7, v7
	v_pk_add_f32 v[0:1], v[0:1], 1.0 op_sel_hi:[1,0]
	v_pk_add_f32 v[2:3], v[2:3], 1.0 op_sel_hi:[1,0]
	v_pk_add_f32 v[4:5], v[4:5], 1.0 op_sel_hi:[1,0]
	v_pk_add_f32 v[6:7], v[6:7], 1.0 op_sel_hi:[1,0]
	v_rcp_f32_e32 v0, v0
	v_rcp_f32_e32 v1, v1
	v_rcp_f32_e32 v2, v2
	v_rcp_f32_e32 v3, v3
	v_rcp_f32_e32 v4, v4
	v_rcp_f32_e32 v5, v5
	v_rcp_f32_e32 v6, v6
	v_rcp_f32_e32 v7, v7
	v_med3_f32 v128, v128, s42, v205
	v_med3_f32 v129, v129, s42, v205
	v_med3_f32 v130, v130, s42, v205
	v_med3_f32 v131, v131, s42, v205
	v_med3_f32 v120, v120, s42, v205
	v_med3_f32 v121, v121, s42, v205
	v_med3_f32 v122, v122, s42, v205
	v_med3_f32 v123, v123, s42, v205
	v_pk_mul_f32 v[0:1], v[0:1], v[132:133]
	v_pk_mul_f32 v[2:3], v[2:3], v[134:135]
	v_pk_mul_f32 v[4:5], v[4:5], v[124:125]
	v_pk_mul_f32 v[6:7], v[6:7], v[126:127]
	v_pk_mul_f32 v[0:1], v[0:1], v[128:129]
	v_pk_mul_f32 v[2:3], v[2:3], v[130:131]
	v_pk_mul_f32 v[4:5], v[4:5], v[120:121]
	v_pk_mul_f32 v[6:7], v[6:7], v[122:123]
	v_cvt_pk_fp8_f32 v220, v0, v1
	v_cvt_pk_fp8_f32 v221, v4, v5
	v_cvt_pk_fp8_f32 v220, v2, v3 op_sel:[0,0,1]
	v_cvt_pk_fp8_f32 v221, v6, v7 op_sel:[0,0,1]
	v_min_f32_e32 v148, s65, v148
	v_min_f32_e32 v149, s65, v149
	v_min_f32_e32 v150, s65, v150
	v_min_f32_e32 v151, s65, v151
	v_min_f32_e32 v140, s65, v140
	v_min_f32_e32 v141, s65, v141
	v_min_f32_e32 v142, s65, v142
	v_min_f32_e32 v143, s65, v143
	v_pk_mul_f32 v[8:9], v[148:149], s[62:63]
	v_pk_mul_f32 v[10:11], v[150:151], s[62:63]
	v_pk_mul_f32 v[12:13], v[140:141], s[62:63]
	v_pk_mul_f32 v[14:15], v[142:143], s[62:63]
	v_exp_f32_e32 v8, v8
	v_exp_f32_e32 v9, v9
	v_exp_f32_e32 v10, v10
	v_exp_f32_e32 v11, v11
	v_exp_f32_e32 v12, v12
	v_exp_f32_e32 v13, v13
	v_exp_f32_e32 v14, v14
	v_exp_f32_e32 v15, v15
	v_pk_add_f32 v[8:9], v[8:9], 1.0 op_sel_hi:[1,0]
	v_pk_add_f32 v[10:11], v[10:11], 1.0 op_sel_hi:[1,0]
	v_pk_add_f32 v[12:13], v[12:13], 1.0 op_sel_hi:[1,0]
	v_pk_add_f32 v[14:15], v[14:15], 1.0 op_sel_hi:[1,0]
	v_rcp_f32_e32 v8, v8
	v_rcp_f32_e32 v9, v9
	v_rcp_f32_e32 v10, v10
	v_rcp_f32_e32 v11, v11
	v_rcp_f32_e32 v12, v12
	v_rcp_f32_e32 v13, v13
	v_rcp_f32_e32 v14, v14
	v_rcp_f32_e32 v15, v15
	v_med3_f32 v144, v144, s42, v205
	v_med3_f32 v145, v145, s42, v205
	v_med3_f32 v146, v146, s42, v205
	v_med3_f32 v147, v147, s42, v205
	v_med3_f32 v136, v136, s42, v205
	v_med3_f32 v137, v137, s42, v205
	v_med3_f32 v138, v138, s42, v205
	v_med3_f32 v139, v139, s42, v205
	v_pk_mul_f32 v[8:9], v[8:9], v[148:149]
	v_pk_mul_f32 v[10:11], v[10:11], v[150:151]
	v_pk_mul_f32 v[12:13], v[12:13], v[140:141]
	v_pk_mul_f32 v[14:15], v[14:15], v[142:143]
	v_pk_mul_f32 v[8:9], v[8:9], v[144:145]
	v_pk_mul_f32 v[10:11], v[10:11], v[146:147]
	v_pk_mul_f32 v[12:13], v[12:13], v[136:137]
	v_pk_mul_f32 v[14:15], v[14:15], v[138:139]
	v_cvt_pk_fp8_f32 v222, v8, v9
	v_cvt_pk_fp8_f32 v223, v12, v13
	v_cvt_pk_fp8_f32 v222, v10, v11 op_sel:[0,0,1]
	v_cvt_pk_fp8_f32 v223, v14, v15 op_sel:[0,0,1]
	s_nop 1
	v_permlane16_swap_b32_e32 v220, v222
	v_permlane16_swap_b32_e32 v221, v223
	global_store_dwordx4 v[16:17], v[220:223], off
	v_lshl_add_u64 v[16:17], v[16:17], 0, s[58:59]
	v_min_f32_e32 v100, s65, v100
	v_min_f32_e32 v101, s65, v101
	v_min_f32_e32 v102, s65, v102
	v_min_f32_e32 v103, s65, v103
	v_min_f32_e32 v92, s65, v92
	v_min_f32_e32 v93, s65, v93
	v_min_f32_e32 v94, s65, v94
	v_min_f32_e32 v95, s65, v95
	v_pk_mul_f32 v[0:1], v[100:101], s[62:63]
	v_pk_mul_f32 v[2:3], v[102:103], s[62:63]
	v_pk_mul_f32 v[4:5], v[92:93], s[62:63]
	v_pk_mul_f32 v[6:7], v[94:95], s[62:63]
	v_exp_f32_e32 v0, v0
	v_exp_f32_e32 v1, v1
	v_exp_f32_e32 v2, v2
	v_exp_f32_e32 v3, v3
	v_exp_f32_e32 v4, v4
	v_exp_f32_e32 v5, v5
	v_exp_f32_e32 v6, v6
	v_exp_f32_e32 v7, v7
	v_pk_add_f32 v[0:1], v[0:1], 1.0 op_sel_hi:[1,0]
	v_pk_add_f32 v[2:3], v[2:3], 1.0 op_sel_hi:[1,0]
	v_pk_add_f32 v[4:5], v[4:5], 1.0 op_sel_hi:[1,0]
	v_pk_add_f32 v[6:7], v[6:7], 1.0 op_sel_hi:[1,0]
	v_rcp_f32_e32 v0, v0
	v_rcp_f32_e32 v1, v1
	v_rcp_f32_e32 v2, v2
	v_rcp_f32_e32 v3, v3
	v_rcp_f32_e32 v4, v4
	v_rcp_f32_e32 v5, v5
	v_rcp_f32_e32 v6, v6
	v_rcp_f32_e32 v7, v7
	v_med3_f32 v96, v96, s42, v205
	v_med3_f32 v97, v97, s42, v205
	v_med3_f32 v98, v98, s42, v205
	v_med3_f32 v99, v99, s42, v205
	v_med3_f32 v88, v88, s42, v205
	v_med3_f32 v89, v89, s42, v205
	v_med3_f32 v90, v90, s42, v205
	v_med3_f32 v91, v91, s42, v205
	v_pk_mul_f32 v[0:1], v[0:1], v[100:101]
	v_pk_mul_f32 v[2:3], v[2:3], v[102:103]
	v_pk_mul_f32 v[4:5], v[4:5], v[92:93]
	v_pk_mul_f32 v[6:7], v[6:7], v[94:95]
	v_pk_mul_f32 v[0:1], v[0:1], v[96:97]
	v_pk_mul_f32 v[2:3], v[2:3], v[98:99]
	v_pk_mul_f32 v[4:5], v[4:5], v[88:89]
	v_pk_mul_f32 v[6:7], v[6:7], v[90:91]
	v_cvt_pk_fp8_f32 v224, v0, v1
	v_cvt_pk_fp8_f32 v225, v4, v5
	v_cvt_pk_fp8_f32 v224, v2, v3 op_sel:[0,0,1]
	v_cvt_pk_fp8_f32 v225, v6, v7 op_sel:[0,0,1]
	v_min_f32_e32 v116, s65, v116
	v_min_f32_e32 v117, s65, v117
	v_min_f32_e32 v118, s65, v118
	v_min_f32_e32 v119, s65, v119
	v_min_f32_e32 v108, s65, v108
	v_min_f32_e32 v109, s65, v109
	v_min_f32_e32 v110, s65, v110
	v_min_f32_e32 v111, s65, v111
	v_pk_mul_f32 v[8:9], v[116:117], s[62:63]
	v_pk_mul_f32 v[10:11], v[118:119], s[62:63]
	v_pk_mul_f32 v[12:13], v[108:109], s[62:63]
	v_pk_mul_f32 v[14:15], v[110:111], s[62:63]
	v_exp_f32_e32 v8, v8
	v_exp_f32_e32 v9, v9
	v_exp_f32_e32 v10, v10
	v_exp_f32_e32 v11, v11
	v_exp_f32_e32 v12, v12
	v_exp_f32_e32 v13, v13
	v_exp_f32_e32 v14, v14
	v_exp_f32_e32 v15, v15
	v_pk_add_f32 v[8:9], v[8:9], 1.0 op_sel_hi:[1,0]
	v_pk_add_f32 v[10:11], v[10:11], 1.0 op_sel_hi:[1,0]
	v_pk_add_f32 v[12:13], v[12:13], 1.0 op_sel_hi:[1,0]
	v_pk_add_f32 v[14:15], v[14:15], 1.0 op_sel_hi:[1,0]
	v_rcp_f32_e32 v8, v8
	v_rcp_f32_e32 v9, v9
	v_rcp_f32_e32 v10, v10
	v_rcp_f32_e32 v11, v11
	v_rcp_f32_e32 v12, v12
	v_rcp_f32_e32 v13, v13
	v_rcp_f32_e32 v14, v14
	v_rcp_f32_e32 v15, v15
	v_med3_f32 v112, v112, s42, v205
	v_med3_f32 v113, v113, s42, v205
	v_med3_f32 v114, v114, s42, v205
	v_med3_f32 v115, v115, s42, v205
	v_med3_f32 v104, v104, s42, v205
	v_med3_f32 v105, v105, s42, v205
	v_med3_f32 v106, v106, s42, v205
	v_med3_f32 v107, v107, s42, v205
	v_pk_mul_f32 v[8:9], v[8:9], v[116:117]
	v_pk_mul_f32 v[10:11], v[10:11], v[118:119]
	v_pk_mul_f32 v[12:13], v[12:13], v[108:109]
	v_pk_mul_f32 v[14:15], v[14:15], v[110:111]
	v_pk_mul_f32 v[8:9], v[8:9], v[112:113]
	v_pk_mul_f32 v[10:11], v[10:11], v[114:115]
	v_pk_mul_f32 v[12:13], v[12:13], v[104:105]
	v_pk_mul_f32 v[14:15], v[14:15], v[106:107]
	v_cvt_pk_fp8_f32 v226, v8, v9
	v_cvt_pk_fp8_f32 v227, v12, v13
	v_cvt_pk_fp8_f32 v226, v10, v11 op_sel:[0,0,1]
	v_cvt_pk_fp8_f32 v227, v14, v15 op_sel:[0,0,1]
	s_nop 1
	v_permlane16_swap_b32_e32 v224, v226
	v_permlane16_swap_b32_e32 v225, v227
	global_store_dwordx4 v[16:17], v[224:227], off
	v_lshl_add_u64 v[16:17], v[16:17], 0, s[60:61]
	v_min_f32_e32 v68, s65, v68
	v_min_f32_e32 v69, s65, v69
	v_min_f32_e32 v70, s65, v70
	v_min_f32_e32 v71, s65, v71
	v_min_f32_e32 v60, s65, v60
	v_min_f32_e32 v61, s65, v61
	v_min_f32_e32 v62, s65, v62
	v_min_f32_e32 v63, s65, v63
	v_pk_mul_f32 v[0:1], v[68:69], s[62:63]
	v_pk_mul_f32 v[2:3], v[70:71], s[62:63]
	v_pk_mul_f32 v[4:5], v[60:61], s[62:63]
	v_pk_mul_f32 v[6:7], v[62:63], s[62:63]
	v_exp_f32_e32 v0, v0
	v_exp_f32_e32 v1, v1
	v_exp_f32_e32 v2, v2
	v_exp_f32_e32 v3, v3
	v_exp_f32_e32 v4, v4
	v_exp_f32_e32 v5, v5
	v_exp_f32_e32 v6, v6
	v_exp_f32_e32 v7, v7
	v_pk_add_f32 v[0:1], v[0:1], 1.0 op_sel_hi:[1,0]
	v_pk_add_f32 v[2:3], v[2:3], 1.0 op_sel_hi:[1,0]
	v_pk_add_f32 v[4:5], v[4:5], 1.0 op_sel_hi:[1,0]
	v_pk_add_f32 v[6:7], v[6:7], 1.0 op_sel_hi:[1,0]
	v_rcp_f32_e32 v0, v0
	v_rcp_f32_e32 v1, v1
	v_rcp_f32_e32 v2, v2
	v_rcp_f32_e32 v3, v3
	v_rcp_f32_e32 v4, v4
	v_rcp_f32_e32 v5, v5
	v_rcp_f32_e32 v6, v6
	v_rcp_f32_e32 v7, v7
	v_med3_f32 v64, v64, s42, v205
	v_med3_f32 v65, v65, s42, v205
	v_med3_f32 v66, v66, s42, v205
	v_med3_f32 v67, v67, s42, v205
	v_med3_f32 v56, v56, s42, v205
	v_med3_f32 v57, v57, s42, v205
	v_med3_f32 v58, v58, s42, v205
	v_med3_f32 v59, v59, s42, v205
	v_pk_mul_f32 v[0:1], v[0:1], v[68:69]
	v_pk_mul_f32 v[2:3], v[2:3], v[70:71]
	v_pk_mul_f32 v[4:5], v[4:5], v[60:61]
	v_pk_mul_f32 v[6:7], v[6:7], v[62:63]
	v_pk_mul_f32 v[0:1], v[0:1], v[64:65]
	v_pk_mul_f32 v[2:3], v[2:3], v[66:67]
	v_pk_mul_f32 v[4:5], v[4:5], v[56:57]
	v_pk_mul_f32 v[6:7], v[6:7], v[58:59]
	v_cvt_pk_fp8_f32 v220, v0, v1
	v_cvt_pk_fp8_f32 v221, v4, v5
	v_cvt_pk_fp8_f32 v220, v2, v3 op_sel:[0,0,1]
	v_cvt_pk_fp8_f32 v221, v6, v7 op_sel:[0,0,1]
	v_min_f32_e32 v84, s65, v84
	v_min_f32_e32 v85, s65, v85
	v_min_f32_e32 v86, s65, v86
	v_min_f32_e32 v87, s65, v87
	v_min_f32_e32 v76, s65, v76
	v_min_f32_e32 v77, s65, v77
	v_min_f32_e32 v78, s65, v78
	v_min_f32_e32 v79, s65, v79
	v_pk_mul_f32 v[8:9], v[84:85], s[62:63]
	v_pk_mul_f32 v[10:11], v[86:87], s[62:63]
	v_pk_mul_f32 v[12:13], v[76:77], s[62:63]
	v_pk_mul_f32 v[14:15], v[78:79], s[62:63]
	v_exp_f32_e32 v8, v8
	v_exp_f32_e32 v9, v9
	v_exp_f32_e32 v10, v10
	v_exp_f32_e32 v11, v11
	v_exp_f32_e32 v12, v12
	v_exp_f32_e32 v13, v13
	v_exp_f32_e32 v14, v14
	v_exp_f32_e32 v15, v15
	v_pk_add_f32 v[8:9], v[8:9], 1.0 op_sel_hi:[1,0]
	v_pk_add_f32 v[10:11], v[10:11], 1.0 op_sel_hi:[1,0]
	v_pk_add_f32 v[12:13], v[12:13], 1.0 op_sel_hi:[1,0]
	v_pk_add_f32 v[14:15], v[14:15], 1.0 op_sel_hi:[1,0]
	v_rcp_f32_e32 v8, v8
	v_rcp_f32_e32 v9, v9
	v_rcp_f32_e32 v10, v10
	v_rcp_f32_e32 v11, v11
	v_rcp_f32_e32 v12, v12
	v_rcp_f32_e32 v13, v13
	v_rcp_f32_e32 v14, v14
	v_rcp_f32_e32 v15, v15
	v_med3_f32 v80, v80, s42, v205
	v_med3_f32 v81, v81, s42, v205
	v_med3_f32 v82, v82, s42, v205
	v_med3_f32 v83, v83, s42, v205
	v_med3_f32 v72, v72, s42, v205
	v_med3_f32 v73, v73, s42, v205
	v_med3_f32 v74, v74, s42, v205
	v_med3_f32 v75, v75, s42, v205
	v_pk_mul_f32 v[8:9], v[8:9], v[84:85]
	v_pk_mul_f32 v[10:11], v[10:11], v[86:87]
	v_pk_mul_f32 v[12:13], v[12:13], v[76:77]
	v_pk_mul_f32 v[14:15], v[14:15], v[78:79]
	v_pk_mul_f32 v[8:9], v[8:9], v[80:81]
	v_pk_mul_f32 v[10:11], v[10:11], v[82:83]
	v_pk_mul_f32 v[12:13], v[12:13], v[72:73]
	v_pk_mul_f32 v[14:15], v[14:15], v[74:75]
	v_cvt_pk_fp8_f32 v222, v8, v9
	v_cvt_pk_fp8_f32 v223, v12, v13
	v_cvt_pk_fp8_f32 v222, v10, v11 op_sel:[0,0,1]
	v_cvt_pk_fp8_f32 v223, v14, v15 op_sel:[0,0,1]
	s_nop 1
	v_permlane16_swap_b32_e32 v220, v222
	v_permlane16_swap_b32_e32 v221, v223
	global_store_dwordx4 v[16:17], v[220:223], off
	v_lshl_add_u64 v[16:17], v[16:17], 0, s[58:59]
	v_min_f32_e32 v36, s65, v36
	v_min_f32_e32 v37, s65, v37
	v_min_f32_e32 v38, s65, v38
	v_min_f32_e32 v39, s65, v39
	v_min_f32_e32 v28, s65, v28
	v_min_f32_e32 v29, s65, v29
	v_min_f32_e32 v30, s65, v30
	v_min_f32_e32 v31, s65, v31
	v_pk_mul_f32 v[0:1], v[36:37], s[62:63]
	v_pk_mul_f32 v[2:3], v[38:39], s[62:63]
	v_pk_mul_f32 v[4:5], v[28:29], s[62:63]
	v_pk_mul_f32 v[6:7], v[30:31], s[62:63]
	v_exp_f32_e32 v0, v0
	v_exp_f32_e32 v1, v1
	v_exp_f32_e32 v2, v2
	v_exp_f32_e32 v3, v3
	v_exp_f32_e32 v4, v4
	v_exp_f32_e32 v5, v5
	v_exp_f32_e32 v6, v6
	v_exp_f32_e32 v7, v7
	v_pk_add_f32 v[0:1], v[0:1], 1.0 op_sel_hi:[1,0]
	v_pk_add_f32 v[2:3], v[2:3], 1.0 op_sel_hi:[1,0]
	v_pk_add_f32 v[4:5], v[4:5], 1.0 op_sel_hi:[1,0]
	v_pk_add_f32 v[6:7], v[6:7], 1.0 op_sel_hi:[1,0]
	v_rcp_f32_e32 v0, v0
	v_rcp_f32_e32 v1, v1
	v_rcp_f32_e32 v2, v2
	v_rcp_f32_e32 v3, v3
	v_rcp_f32_e32 v4, v4
	v_rcp_f32_e32 v5, v5
	v_rcp_f32_e32 v6, v6
	v_rcp_f32_e32 v7, v7
	v_med3_f32 v32, v32, s42, v205
	v_med3_f32 v33, v33, s42, v205
	v_med3_f32 v34, v34, s42, v205
	v_med3_f32 v35, v35, s42, v205
	v_med3_f32 v24, v24, s42, v205
	v_med3_f32 v25, v25, s42, v205
	v_med3_f32 v26, v26, s42, v205
	v_med3_f32 v27, v27, s42, v205
	v_pk_mul_f32 v[0:1], v[0:1], v[36:37]
	v_pk_mul_f32 v[2:3], v[2:3], v[38:39]
	v_pk_mul_f32 v[4:5], v[4:5], v[28:29]
	v_pk_mul_f32 v[6:7], v[6:7], v[30:31]
	v_pk_mul_f32 v[0:1], v[0:1], v[32:33]
	v_pk_mul_f32 v[2:3], v[2:3], v[34:35]
	v_pk_mul_f32 v[4:5], v[4:5], v[24:25]
	v_pk_mul_f32 v[6:7], v[6:7], v[26:27]
	v_cvt_pk_fp8_f32 v224, v0, v1
	v_cvt_pk_fp8_f32 v225, v4, v5
	v_cvt_pk_fp8_f32 v224, v2, v3 op_sel:[0,0,1]
	v_cvt_pk_fp8_f32 v225, v6, v7 op_sel:[0,0,1]
	v_min_f32_e32 v52, s65, v52
	v_min_f32_e32 v53, s65, v53
	v_min_f32_e32 v54, s65, v54
	v_min_f32_e32 v55, s65, v55
	v_min_f32_e32 v44, s65, v44
	v_min_f32_e32 v45, s65, v45
	v_min_f32_e32 v46, s65, v46
	v_min_f32_e32 v47, s65, v47
	v_pk_mul_f32 v[8:9], v[52:53], s[62:63]
	v_pk_mul_f32 v[10:11], v[54:55], s[62:63]
	v_pk_mul_f32 v[12:13], v[44:45], s[62:63]
	v_pk_mul_f32 v[14:15], v[46:47], s[62:63]
	v_exp_f32_e32 v8, v8
	v_exp_f32_e32 v9, v9
	v_exp_f32_e32 v10, v10
	v_exp_f32_e32 v11, v11
	v_exp_f32_e32 v12, v12
	v_exp_f32_e32 v13, v13
	v_exp_f32_e32 v14, v14
	v_exp_f32_e32 v15, v15
	v_pk_add_f32 v[8:9], v[8:9], 1.0 op_sel_hi:[1,0]
	v_pk_add_f32 v[10:11], v[10:11], 1.0 op_sel_hi:[1,0]
	v_pk_add_f32 v[12:13], v[12:13], 1.0 op_sel_hi:[1,0]
	v_pk_add_f32 v[14:15], v[14:15], 1.0 op_sel_hi:[1,0]
	v_rcp_f32_e32 v8, v8
	v_rcp_f32_e32 v9, v9
	v_rcp_f32_e32 v10, v10
	v_rcp_f32_e32 v11, v11
	v_rcp_f32_e32 v12, v12
	v_rcp_f32_e32 v13, v13
	v_rcp_f32_e32 v14, v14
	v_rcp_f32_e32 v15, v15
	v_med3_f32 v48, v48, s42, v205
	v_med3_f32 v49, v49, s42, v205
	v_med3_f32 v50, v50, s42, v205
	v_med3_f32 v51, v51, s42, v205
	v_med3_f32 v40, v40, s42, v205
	v_med3_f32 v41, v41, s42, v205
	v_med3_f32 v42, v42, s42, v205
	v_med3_f32 v43, v43, s42, v205
	v_pk_mul_f32 v[8:9], v[8:9], v[52:53]
	v_pk_mul_f32 v[10:11], v[10:11], v[54:55]
	v_pk_mul_f32 v[12:13], v[12:13], v[44:45]
	v_pk_mul_f32 v[14:15], v[14:15], v[46:47]
	v_pk_mul_f32 v[8:9], v[8:9], v[48:49]
	v_pk_mul_f32 v[10:11], v[10:11], v[50:51]
	v_pk_mul_f32 v[12:13], v[12:13], v[40:41]
	v_pk_mul_f32 v[14:15], v[14:15], v[42:43]
	v_cvt_pk_fp8_f32 v226, v8, v9
	v_cvt_pk_fp8_f32 v227, v12, v13
	v_cvt_pk_fp8_f32 v226, v10, v11 op_sel:[0,0,1]
	v_cvt_pk_fp8_f32 v227, v14, v15 op_sel:[0,0,1]
	s_nop 1
	v_permlane16_swap_b32_e32 v224, v226
	v_permlane16_swap_b32_e32 v225, v227
	global_store_dwordx4 v[16:17], v[224:227], off
	s_mov_b32 s52, s49
	s_mov_b32 s51, s47
	s_mov_b32 s50, s48
	v_mov_b32_e32 v162, v160
	v_mov_b32_e32 v164, v158
	v_mov_b32_e32 v166, v207
	v_mov_b32_e32 v208, v206
	s_mov_b64 s[16:17], s[14:15]
	s_and_b64 vcc, exec, s[12:13]
	s_cbranch_vccnz .LBB0_1338

.LBB0_1334:
	s_add_u32 s16, s16, 0x100
	v_mov_b32_e32 v165, v157
	v_mov_b32_e32 v163, v157
	v_mov_b32_e32 v159, v157
	v_mov_b32_e32 v161, v157
	s_addc_u32 s17, s17, 0
	s_mov_b32 s53, -2
	s_mov_b64 s[18:19], s[8:9]
	v_lshl_add_u32 v16, s52, 10, v188
	ds_read_b128 v[0:3], v16
	ds_read_b128 v[4:7], v16 offset:16
	ds_read_b128 v[8:11], v16 offset:512
	ds_read_b128 v[12:15], v16 offset:528
	s_waitcnt lgkmcnt(0)
	v_fma_f32 v8, v8, 4.0, 4.0
	v_fma_f32 v9, v9, 4.0, 4.0
	v_fma_f32 v10, v10, 4.0, 4.0
	v_fma_f32 v11, v11, 4.0, 4.0
	v_fma_f32 v12, v12, 4.0, 4.0
	v_fma_f32 v13, v13, 4.0, 4.0
	v_fma_f32 v14, v14, 4.0, 4.0
	v_fma_f32 v15, v15, 4.0, 4.0
	v_mov_b32_e32 v148, v0
	v_mov_b32_e32 v144, v8
	v_mov_b32_e32 v149, v1
	v_mov_b32_e32 v145, v9
	v_mov_b32_e32 v150, v2
	v_mov_b32_e32 v146, v10
	v_mov_b32_e32 v151, v3
	v_mov_b32_e32 v147, v11
	v_mov_b32_e32 v140, v4
	v_mov_b32_e32 v136, v12
	v_mov_b32_e32 v141, v5
	v_mov_b32_e32 v137, v13
	v_mov_b32_e32 v142, v6
	v_mov_b32_e32 v138, v14
	v_mov_b32_e32 v143, v7
	v_mov_b32_e32 v139, v15
	v_mov_b32_e32 v132, v0
	v_mov_b32_e32 v128, v8
	v_mov_b32_e32 v133, v1
	v_mov_b32_e32 v129, v9
	v_mov_b32_e32 v134, v2
	v_mov_b32_e32 v130, v10
	v_mov_b32_e32 v135, v3
	v_mov_b32_e32 v131, v11
	v_mov_b32_e32 v124, v4
	v_mov_b32_e32 v120, v12
	v_mov_b32_e32 v125, v5
	v_mov_b32_e32 v121, v13
	v_mov_b32_e32 v126, v6
	v_mov_b32_e32 v122, v14
	v_mov_b32_e32 v127, v7
	v_mov_b32_e32 v123, v15
	v_mov_b32_e32 v116, v0
	v_mov_b32_e32 v112, v8
	v_mov_b32_e32 v117, v1
	v_mov_b32_e32 v113, v9
	v_mov_b32_e32 v118, v2
	v_mov_b32_e32 v114, v10
	v_mov_b32_e32 v119, v3
	v_mov_b32_e32 v115, v11
	v_mov_b32_e32 v108, v4
	v_mov_b32_e32 v104, v12
	v_mov_b32_e32 v109, v5
	v_mov_b32_e32 v105, v13
	v_mov_b32_e32 v110, v6
	v_mov_b32_e32 v106, v14
	v_mov_b32_e32 v111, v7
	v_mov_b32_e32 v107, v15
	v_mov_b32_e32 v100, v0
	v_mov_b32_e32 v96, v8
	v_mov_b32_e32 v101, v1
	v_mov_b32_e32 v97, v9
	v_mov_b32_e32 v102, v2
	v_mov_b32_e32 v98, v10
	v_mov_b32_e32 v103, v3
	v_mov_b32_e32 v99, v11
	v_mov_b32_e32 v92, v4
	v_mov_b32_e32 v88, v12
	v_mov_b32_e32 v93, v5
	v_mov_b32_e32 v89, v13
	v_mov_b32_e32 v94, v6
	v_mov_b32_e32 v90, v14
	v_mov_b32_e32 v95, v7
	v_mov_b32_e32 v91, v15
	v_mov_b32_e32 v84, v0
	v_mov_b32_e32 v80, v8
	v_mov_b32_e32 v85, v1
	v_mov_b32_e32 v81, v9
	v_mov_b32_e32 v86, v2
	v_mov_b32_e32 v82, v10
	v_mov_b32_e32 v87, v3
	v_mov_b32_e32 v83, v11
	v_mov_b32_e32 v76, v4
	v_mov_b32_e32 v72, v12
	v_mov_b32_e32 v77, v5
	v_mov_b32_e32 v73, v13
	v_mov_b32_e32 v78, v6
	v_mov_b32_e32 v74, v14
	v_mov_b32_e32 v79, v7
	v_mov_b32_e32 v75, v15
	v_mov_b32_e32 v68, v0
	v_mov_b32_e32 v64, v8
	v_mov_b32_e32 v69, v1
	v_mov_b32_e32 v65, v9
	v_mov_b32_e32 v70, v2
	v_mov_b32_e32 v66, v10
	v_mov_b32_e32 v71, v3
	v_mov_b32_e32 v67, v11
	v_mov_b32_e32 v60, v4
	v_mov_b32_e32 v56, v12
	v_mov_b32_e32 v61, v5
	v_mov_b32_e32 v57, v13
	v_mov_b32_e32 v62, v6
	v_mov_b32_e32 v58, v14
	v_mov_b32_e32 v63, v7
	v_mov_b32_e32 v59, v15
	v_mov_b32_e32 v52, v0
	v_mov_b32_e32 v48, v8
	v_mov_b32_e32 v53, v1
	v_mov_b32_e32 v49, v9
	v_mov_b32_e32 v54, v2
	v_mov_b32_e32 v50, v10
	v_mov_b32_e32 v55, v3
	v_mov_b32_e32 v51, v11
	v_mov_b32_e32 v44, v4
	v_mov_b32_e32 v40, v12
	v_mov_b32_e32 v45, v5
	v_mov_b32_e32 v41, v13
	v_mov_b32_e32 v46, v6
	v_mov_b32_e32 v42, v14
	v_mov_b32_e32 v47, v7
	v_mov_b32_e32 v43, v15
	v_mov_b32_e32 v36, v0
	v_mov_b32_e32 v32, v8
	v_mov_b32_e32 v37, v1
	v_mov_b32_e32 v33, v9
	v_mov_b32_e32 v38, v2
	v_mov_b32_e32 v34, v10
	v_mov_b32_e32 v39, v3
	v_mov_b32_e32 v35, v11
	v_mov_b32_e32 v28, v4
	v_mov_b32_e32 v24, v12
	v_mov_b32_e32 v29, v5
	v_mov_b32_e32 v25, v13
	v_mov_b32_e32 v30, v6
	v_mov_b32_e32 v26, v14
	v_mov_b32_e32 v31, v7
	v_mov_b32_e32 v27, v15
	s_branch .LBB0_1336
.LBB0_1335:
	ds_read_b128 v[0:3], v184
	ds_read_b128 v[4:7], v189
	ds_read_b128 v[8:11], v190
	ds_read_b128 v[12:15], v191
	s_add_u32 s54, s18, 0x80
	s_addc_u32 s55, s19, 0
	s_and_b64 s[22:23], exec, s[22:23]
	s_cselect_b32 s23, s1, s55
	s_cselect_b32 s22, s0, s54
	v_lshl_add_u64 v[16:17], s[18:19], 0, v[164:165]
	s_add_i32 m0, s27, 0xc000
	ds_read_b128 v[210:213], v202
	ds_read_b128 v[214:217], v202 offset:1024
	ds_read_b128 v[218:221], v202 offset:2048
	ds_read_b128 v[222:225], v202 offset:3072
	ds_read_b128 v[226:229], v202 offset:4096
	ds_read_b128 v[230:233], v202 offset:5120
	ds_read_b128 v[234:237], v202 offset:6144
	ds_read_b128 v[238:241], v202 offset:7168
	global_load_lds_dwordx4 v[16:17], off
	v_lshl_add_u64 v[16:17], s[18:19], 0, v[162:163]
	s_add_i32 m0, s27, 0xe000
	s_nop 0
	global_load_lds_dwordx4 v[16:17], off
	s_waitcnt lgkmcnt(8)
	s_barrier
	s_waitcnt lgkmcnt(0)
	s_setprio 1
	s_waitcnt lgkmcnt(0)
	v_mfma_scale_f32_16x16x128_f8f6f4 v[148:151], v[0:7], v[210:217], v[148:151], v203, v204 op_sel_hi:[0,0,0]
	v_mfma_scale_f32_16x16x128_f8f6f4 v[140:143], v[8:15], v[210:217], v[140:143], v203, v204 op_sel_hi:[0,0,0]
	v_mfma_scale_f32_16x16x128_f8f6f4 v[132:135], v[0:7], v[218:225], v[132:135], v203, v204 op_sel_hi:[0,0,0]
	v_mfma_scale_f32_16x16x128_f8f6f4 v[124:127], v[8:15], v[218:225], v[124:127], v203, v204 op_sel_hi:[0,0,0]
	v_mfma_scale_f32_16x16x128_f8f6f4 v[116:119], v[0:7], v[226:233], v[116:119], v203, v204 op_sel_hi:[0,0,0]
	v_mfma_scale_f32_16x16x128_f8f6f4 v[108:111], v[8:15], v[226:233], v[108:111], v203, v204 op_sel_hi:[0,0,0]
	v_mfma_scale_f32_16x16x128_f8f6f4 v[100:103], v[0:7], v[234:241], v[100:103], v203, v204 op_sel_hi:[0,0,0]
	v_mfma_scale_f32_16x16x128_f8f6f4 v[92:95], v[8:15], v[234:241], v[92:95], v203, v204 op_sel_hi:[0,0,0]
	s_setprio 0
	s_barrier
	s_mov_b32 m0, s28
	v_lshl_add_u64 v[172:173], s[20:21], 0, v[154:155]
	ds_read_b128 v[16:19], v185
	ds_read_b128 v[20:23], v192
	ds_read_b128 v[242:245], v193
	ds_read_b128 v[246:249], v194
	global_load_lds_dwordx4 v[172:173], off
	v_lshl_add_u64 v[174:175], s[20:21], 0, v[152:153]
	s_mov_b32 m0, s29
	s_nop 0
	global_load_lds_dwordx4 v[174:175], off
	s_barrier
	s_waitcnt lgkmcnt(0)
	s_setprio 1
	s_waitcnt lgkmcnt(0)
	v_mfma_scale_f32_16x16x128_f8f6f4 v[144:147], v[16:23], v[210:217], v[144:147], v209, v204 op_sel_hi:[0,0,0]
	v_mfma_scale_f32_16x16x128_f8f6f4 v[136:139], v[242:249], v[210:217], v[136:139], v209, v204 op_sel_hi:[0,0,0]
	v_mfma_scale_f32_16x16x128_f8f6f4 v[128:131], v[16:23], v[218:225], v[128:131], v209, v204 op_sel_hi:[0,0,0]
	v_mfma_scale_f32_16x16x128_f8f6f4 v[120:123], v[242:249], v[218:225], v[120:123], v209, v204 op_sel_hi:[0,0,0]
	v_mfma_scale_f32_16x16x128_f8f6f4 v[112:115], v[16:23], v[226:233], v[112:115], v209, v204 op_sel_hi:[0,0,0]
	v_mfma_scale_f32_16x16x128_f8f6f4 v[104:107], v[242:249], v[226:233], v[104:107], v209, v204 op_sel_hi:[0,0,0]
	v_mfma_scale_f32_16x16x128_f8f6f4 v[96:99], v[16:23], v[234:241], v[96:99], v209, v204 op_sel_hi:[0,0,0]
	v_mfma_scale_f32_16x16x128_f8f6f4 v[88:91], v[242:249], v[234:241], v[88:91], v209, v204 op_sel_hi:[0,0,0]
	s_setprio 0
	s_mov_b32 m0, s27
	s_barrier
	ds_read_b128 v[210:213], v202 offset:16384
	ds_read_b128 v[214:217], v202 offset:17408
	ds_read_b128 v[218:221], v202 offset:18432
	ds_read_b128 v[222:225], v202 offset:19456
	ds_read_b128 v[226:229], v202 offset:20480
	ds_read_b128 v[230:233], v202 offset:21504
	ds_read_b128 v[234:237], v202 offset:22528
	ds_read_b128 v[238:241], v202 offset:23552
	global_load_lds_dwordx4 v156, s[22:23]
	s_mov_b32 m0, s30
	v_mov_b32_e32 v177, v157
	global_load_lds_dwordx4 v176, s[22:23]
	s_barrier
	s_waitcnt lgkmcnt(0)
	v_lshl_add_u64 v[178:179], s[22:23], 0, v[156:157]
	v_lshl_add_u64 v[176:177], s[22:23], 0, v[176:177]
	s_setprio 1
	s_waitcnt lgkmcnt(0)
	v_mfma_scale_f32_16x16x128_f8f6f4 v[84:87], v[0:7], v[210:217], v[84:87], v203, v204 op_sel_hi:[0,0,0]
	v_mfma_scale_f32_16x16x128_f8f6f4 v[76:79], v[8:15], v[210:217], v[76:79], v203, v204 op_sel_hi:[0,0,0]
	v_mfma_scale_f32_16x16x128_f8f6f4 v[68:71], v[0:7], v[218:225], v[68:71], v203, v204 op_sel_hi:[0,0,0]
	v_mfma_scale_f32_16x16x128_f8f6f4 v[60:63], v[8:15], v[218:225], v[60:63], v203, v204 op_sel_hi:[0,0,0]
	v_mfma_scale_f32_16x16x128_f8f6f4 v[52:55], v[0:7], v[226:233], v[52:55], v203, v204 op_sel_hi:[0,0,0]
	v_mfma_scale_f32_16x16x128_f8f6f4 v[44:47], v[8:15], v[226:233], v[44:47], v203, v204 op_sel_hi:[0,0,0]
	v_mfma_scale_f32_16x16x128_f8f6f4 v[36:39], v[0:7], v[234:241], v[36:39], v203, v204 op_sel_hi:[0,0,0]
	v_mfma_scale_f32_16x16x128_f8f6f4 v[28:31], v[8:15], v[234:241], v[28:31], v203, v204 op_sel_hi:[0,0,0]
	s_setprio 0
	s_barrier
	s_add_u32 s54, s20, 0x40000
	s_addc_u32 s55, s21, 0
	s_mov_b32 m0, s31
	v_lshl_add_u64 v[0:1], s[54:55], 0, v[154:155]
	global_load_lds_dwordx4 v[0:1], off
	v_lshl_add_u64 v[0:1], s[54:55], 0, v[152:153]
	s_mov_b32 m0, s33
	s_nop 0
	global_load_lds_dwordx4 v[0:1], off
	s_waitcnt vmcnt(6)
	s_barrier
	s_setprio 1
	v_mfma_scale_f32_16x16x128_f8f6f4 v[80:83], v[16:23], v[210:217], v[80:83], v209, v204 op_sel_hi:[0,0,0]
	v_mfma_scale_f32_16x16x128_f8f6f4 v[72:75], v[242:249], v[210:217], v[72:75], v209, v204 op_sel_hi:[0,0,0]
	v_mfma_scale_f32_16x16x128_f8f6f4 v[64:67], v[16:23], v[218:225], v[64:67], v209, v204 op_sel_hi:[0,0,0]
	v_mfma_scale_f32_16x16x128_f8f6f4 v[56:59], v[242:249], v[218:225], v[56:59], v209, v204 op_sel_hi:[0,0,0]
	v_mfma_scale_f32_16x16x128_f8f6f4 v[48:51], v[16:23], v[226:233], v[48:51], v209, v204 op_sel_hi:[0,0,0]
	v_mfma_scale_f32_16x16x128_f8f6f4 v[40:43], v[242:249], v[226:233], v[40:43], v209, v204 op_sel_hi:[0,0,0]
	v_mfma_scale_f32_16x16x128_f8f6f4 v[32:35], v[16:23], v[234:241], v[32:35], v209, v204 op_sel_hi:[0,0,0]
	v_mfma_scale_f32_16x16x128_f8f6f4 v[24:27], v[242:249], v[234:241], v[24:27], v209, v204 op_sel_hi:[0,0,0]
	s_setprio 0
	s_barrier
	ds_read_b128 v[0:3], v186
	ds_read_b128 v[4:7], v195
	ds_read_b128 v[8:11], v196
	ds_read_b128 v[12:15], v197
	s_mov_b32 m0, s34
	v_lshl_add_u64 v[170:171], s[22:23], 0, v[170:171]
	ds_read_b128 v[16:19], v202 offset:32768
	ds_read_b128 v[20:23], v202 offset:33792
	ds_read_b128 v[210:213], v202 offset:34816
	ds_read_b128 v[214:217], v202 offset:35840
	ds_read_b128 v[218:221], v202 offset:36864
	ds_read_b128 v[222:225], v202 offset:37888
	ds_read_b128 v[226:229], v202 offset:38912
	ds_read_b128 v[230:233], v202 offset:39936
	global_load_lds_dwordx4 v[170:171], off
	v_lshl_add_u64 v[168:169], s[22:23], 0, v[168:169]
	s_mov_b32 m0, s35
	s_nop 0
	global_load_lds_dwordx4 v[168:169], off
	s_waitcnt lgkmcnt(8)
	s_barrier
	s_waitcnt lgkmcnt(0)
	s_setprio 1
	s_waitcnt lgkmcnt(0)
	v_mfma_scale_f32_16x16x128_f8f6f4 v[148:151], v[0:7], v[16:23], v[148:151], v203, v204 op_sel_hi:[0,0,0]
	v_mfma_scale_f32_16x16x128_f8f6f4 v[140:143], v[8:15], v[16:23], v[140:143], v203, v204 op_sel_hi:[0,0,0]
	v_mfma_scale_f32_16x16x128_f8f6f4 v[132:135], v[0:7], v[210:217], v[132:135], v203, v204 op_sel_hi:[0,0,0]
	v_mfma_scale_f32_16x16x128_f8f6f4 v[124:127], v[8:15], v[210:217], v[124:127], v203, v204 op_sel_hi:[0,0,0]
	v_mfma_scale_f32_16x16x128_f8f6f4 v[116:119], v[0:7], v[218:225], v[116:119], v203, v204 op_sel_hi:[0,0,0]
	v_mfma_scale_f32_16x16x128_f8f6f4 v[108:111], v[8:15], v[218:225], v[108:111], v203, v204 op_sel_hi:[0,0,0]
	v_mfma_scale_f32_16x16x128_f8f6f4 v[100:103], v[0:7], v[226:233], v[100:103], v203, v204 op_sel_hi:[0,0,0]
	v_mfma_scale_f32_16x16x128_f8f6f4 v[92:95], v[8:15], v[226:233], v[92:95], v203, v204 op_sel_hi:[0,0,0]
	s_setprio 0
	s_barrier
	s_mov_b32 m0, s36
	v_lshl_add_u64 v[168:169], v[172:173], 0, s[10:11]
	ds_read_b128 v[234:237], v187
	ds_read_b128 v[238:241], v198
	ds_read_b128 v[242:245], v199
	ds_read_b128 v[246:249], v200
	global_load_lds_dwordx4 v[168:169], off
	v_lshl_add_u64 v[168:169], v[174:175], 0, s[10:11]
	s_mov_b32 m0, s37
	s_nop 0
	global_load_lds_dwordx4 v[168:169], off
	s_barrier
	s_waitcnt lgkmcnt(0)
	s_setprio 1
	s_waitcnt lgkmcnt(0)
	v_mfma_scale_f32_16x16x128_f8f6f4 v[144:147], v[234:241], v[16:23], v[144:147], v209, v204 op_sel_hi:[0,0,0]
	v_mfma_scale_f32_16x16x128_f8f6f4 v[136:139], v[242:249], v[16:23], v[136:139], v209, v204 op_sel_hi:[0,0,0]
	v_mfma_scale_f32_16x16x128_f8f6f4 v[128:131], v[234:241], v[210:217], v[128:131], v209, v204 op_sel_hi:[0,0,0]
	v_mfma_scale_f32_16x16x128_f8f6f4 v[120:123], v[242:249], v[210:217], v[120:123], v209, v204 op_sel_hi:[0,0,0]
	v_mfma_scale_f32_16x16x128_f8f6f4 v[112:115], v[234:241], v[218:225], v[112:115], v209, v204 op_sel_hi:[0,0,0]
	v_mfma_scale_f32_16x16x128_f8f6f4 v[104:107], v[242:249], v[218:225], v[104:107], v209, v204 op_sel_hi:[0,0,0]
	v_mfma_scale_f32_16x16x128_f8f6f4 v[96:99], v[234:241], v[226:233], v[96:99], v209, v204 op_sel_hi:[0,0,0]
	v_mfma_scale_f32_16x16x128_f8f6f4 v[88:91], v[242:249], v[226:233], v[88:91], v209, v204 op_sel_hi:[0,0,0]
	s_setprio 0
	s_mov_b32 m0, s38
	v_lshl_add_u64 v[178:179], v[178:179], 0, s[10:11]
	s_barrier
	ds_read_b128 v[16:19], v202 offset:49152
	ds_read_b128 v[20:23], v202 offset:50176
	ds_read_b128 v[168:171], v202 offset:51200
	ds_read_b128 v[172:175], v202 offset:52224
	ds_read_b128 v[210:213], v202 offset:53248
	ds_read_b128 v[214:217], v202 offset:54272
	ds_read_b128 v[218:221], v202 offset:55296
	ds_read_b128 v[222:225], v202 offset:56320
	global_load_lds_dwordx4 v[178:179], off
	v_lshl_add_u64 v[176:177], v[176:177], 0, s[10:11]
	s_mov_b32 m0, s39
	s_nop 0
	global_load_lds_dwordx4 v[176:177], off
	s_barrier
	s_waitcnt lgkmcnt(0)
	s_setprio 1
	s_waitcnt lgkmcnt(0)
	v_mfma_scale_f32_16x16x128_f8f6f4 v[84:87], v[0:7], v[16:23], v[84:87], v203, v204 op_sel_hi:[0,0,0]
	v_mfma_scale_f32_16x16x128_f8f6f4 v[76:79], v[8:15], v[16:23], v[76:79], v203, v204 op_sel_hi:[0,0,0]
	v_mfma_scale_f32_16x16x128_f8f6f4 v[68:71], v[0:7], v[168:175], v[68:71], v203, v204 op_sel_hi:[0,0,0]
	v_mfma_scale_f32_16x16x128_f8f6f4 v[60:63], v[8:15], v[168:175], v[60:63], v203, v204 op_sel_hi:[0,0,0]
	v_mfma_scale_f32_16x16x128_f8f6f4 v[52:55], v[0:7], v[210:217], v[52:55], v203, v204 op_sel_hi:[0,0,0]
	v_mfma_scale_f32_16x16x128_f8f6f4 v[44:47], v[8:15], v[210:217], v[44:47], v203, v204 op_sel_hi:[0,0,0]
	v_mfma_scale_f32_16x16x128_f8f6f4 v[36:39], v[0:7], v[218:225], v[36:39], v203, v204 op_sel_hi:[0,0,0]
	v_mfma_scale_f32_16x16x128_f8f6f4 v[28:31], v[8:15], v[218:225], v[28:31], v203, v204 op_sel_hi:[0,0,0]
	s_setprio 0
	s_barrier
	s_add_u32 s20, s20, 0x40080
	s_addc_u32 s21, s21, 0
	s_mov_b32 m0, s40
	v_lshl_add_u64 v[0:1], s[20:21], 0, v[154:155]
	global_load_lds_dwordx4 v[0:1], off
	v_lshl_add_u64 v[0:1], s[20:21], 0, v[152:153]
	s_mov_b32 m0, s41
	s_nop 0
	global_load_lds_dwordx4 v[0:1], off
	s_waitcnt vmcnt(6)
	s_barrier
	s_setprio 1
	v_mfma_scale_f32_16x16x128_f8f6f4 v[80:83], v[234:241], v[16:23], v[80:83], v209, v204 op_sel_hi:[0,0,0]
	v_mfma_scale_f32_16x16x128_f8f6f4 v[72:75], v[242:249], v[16:23], v[72:75], v209, v204 op_sel_hi:[0,0,0]
	v_mfma_scale_f32_16x16x128_f8f6f4 v[64:67], v[234:241], v[168:175], v[64:67], v209, v204 op_sel_hi:[0,0,0]
	v_mfma_scale_f32_16x16x128_f8f6f4 v[56:59], v[242:249], v[168:175], v[56:59], v209, v204 op_sel_hi:[0,0,0]
	v_mfma_scale_f32_16x16x128_f8f6f4 v[48:51], v[234:241], v[210:217], v[48:51], v209, v204 op_sel_hi:[0,0,0]
	v_mfma_scale_f32_16x16x128_f8f6f4 v[40:43], v[242:249], v[210:217], v[40:43], v209, v204 op_sel_hi:[0,0,0]
	v_mfma_scale_f32_16x16x128_f8f6f4 v[32:35], v[234:241], v[218:225], v[32:35], v209, v204 op_sel_hi:[0,0,0]
	v_mfma_scale_f32_16x16x128_f8f6f4 v[24:27], v[242:249], v[218:225], v[24:27], v209, v204 op_sel_hi:[0,0,0]
	s_setprio 0
	s_add_i32 s53, s53, 2
	s_add_u32 s18, s18, 0x100
	s_addc_u32 s19, s19, 0
	s_add_u32 s16, s16, 0x100
	s_addc_u32 s17, s17, 0
	s_cmp_gt_u32 s53, 13
	s_barrier
	s_cbranch_scc1 .LBB0_1326
